# P9: during a unit's epilogue every thread touches one line of K-tiles 2/3 of the next unit's A and B tiles (plain loads to an unused VGPR) so the next unit's short-lead LDS-DMA loads hit the L2
# baseline (speedup 1.0000x reference)
.LBB0_1668:
	s_waitcnt lgkmcnt(0)
	s_cmp_lt_u32 s40, s30
	s_cbranch_scc0 .Lmy_p9pf
	v_readfirstlane_b32 s98, v178
	v_lshrrev_b32_e32 v253, 1, v0
	v_and_b32_e32 v254, 1, v0
	v_lshlrev_b32_e32 v253, 9, v253
	v_lshl_add_u32 v253, v254, 7, v253
	s_mov_b32 s99, 0
	s_lshl_b64 s[98:99], s[98:99], 17
	s_add_u32 s98, s12, s98
	s_addc_u32 s99, s13, s99
	global_load_dword v254, v253, s[18:19] offset:256
	global_load_dword v254, v253, s[98:99] offset:256
